# counted wait on the P4 token-mixing critical path: the bias wait leaves the next unit's 8 prefetch loads in flight (vmcnt(8) instead of vmcnt(0))
# speedup vs baseline: 1.0269x; 1.0004x over previous
.LBB0_564:
	s_mov_b32 s98, 0
	s_cmpk_gt_i32 s87, 0x5bf
	s_cbranch_scc1 .LBB0_569
	v_mov_b32_e32 v53, v0
	s_cmpk_gt_i32 s87, 0x3bf
	s_mov_b64 s[42:43], -1
	s_cbranch_scc0 .LBB0_567
	s_lshr_b32 s12, s86, 7
	s_lshl_b64 s[30:31], s[12:13], 11
	s_and_b32 s12, s46, 0x780
	s_or_b32 s30, s30, s12
	s_add_i32 s12, s47, 0x8000
	s_and_b32 s12, s12, 0x700
	v_ashrrev_i32_e32 v54, 4, v53
	s_lshl_b32 s12, s12, 1
	v_ashrrev_i32_e32 v55, 31, v54
	s_add_u32 s34, s58, s12
	v_lshl_add_u64 v[54:55], s[30:31], 0, v[54:55]
	s_addc_u32 s35, s59, 0
	v_lshlrev_b64 v[54:55], 12, v[54:55]
	v_lshlrev_b32_e32 v56, 4, v53
	v_lshl_add_u64 v[54:55], s[34:35], 0, v[54:55]
	v_and_b32_e32 v56, 0xf0, v56
	v_mov_b32_e32 v57, v163
	v_lshl_add_u64 v[58:59], v[54:55], 0, v[56:57]
	v_add_u32_e32 v54, 0x200, v53
	v_ashrrev_i32_e32 v54, 4, v54
	v_ashrrev_i32_e32 v55, 31, v54
	v_lshl_add_u64 v[54:55], s[30:31], 0, v[54:55]
	v_lshlrev_b64 v[54:55], 12, v[54:55]
	v_lshl_add_u64 v[54:55], s[34:35], 0, v[54:55]
	v_lshl_add_u64 v[60:61], v[54:55], 0, v[56:57]
	v_add_u32_e32 v54, 0x400, v53
	v_ashrrev_i32_e32 v54, 4, v54
	v_ashrrev_i32_e32 v55, 31, v54
	v_lshl_add_u64 v[54:55], s[30:31], 0, v[54:55]
	v_lshlrev_b64 v[54:55], 12, v[54:55]
	v_lshl_add_u64 v[54:55], s[34:35], 0, v[54:55]
	v_lshl_add_u64 v[70:71], v[54:55], 0, v[56:57]
	v_add_u32_e32 v54, 0x600, v53
	v_ashrrev_i32_e32 v54, 4, v54
	v_ashrrev_i32_e32 v55, 31, v54
	v_lshl_add_u64 v[54:55], s[30:31], 0, v[54:55]
	v_lshlrev_b64 v[54:55], 12, v[54:55]
	v_lshl_add_u64 v[54:55], s[34:35], 0, v[54:55]
	v_lshl_add_u64 v[88:89], v[54:55], 0, v[56:57]
	global_load_dwordx4 v[54:57], v[58:59], off
	global_load_dwordx4 v[62:65], v[58:59], off offset:256
	global_load_dwordx4 v[74:77], v[60:61], off
	global_load_dwordx4 v[66:69], v[60:61], off offset:256
	global_load_dwordx4 v[78:81], v[70:71], off
	s_nop 0
	global_load_dwordx4 v[70:73], v[70:71], off offset:256
	s_nop 0
	global_load_dwordx4 v[82:85], v[88:89], off
	global_load_dwordx4 v[58:61], v[88:89], off offset:256
	s_mov_b64 s[42:43], 0
	s_mov_b32 s98, 1

.LBB0_569:
	v_lshlrev_b32_e32 v53, 11, v86
	v_lshlrev_b32_e32 v86, 1, v86
	v_lshlrev_b32_e32 v87, 6, v200
	v_bfe_u32 v220, v201, 1, 1
	v_and_b32_e32 v88, 12, v201
	v_and_b32_e32 v219, 2, v86
	v_lshlrev_b32_e32 v89, 3, v201
	v_and_b32_e32 v87, 0x300, v87
	v_lshrrev_b32_e32 v221, 1, v201
	v_or_b32_e32 v86, v219, v88
	v_and_b32_e32 v89, 8, v89
	v_or_b32_e32 v90, 2, v220
	v_or_b32_e32 v92, 4, v220
	v_or_b32_e32 v94, 6, v220
	v_or_b32_e32 v96, 8, v220
	v_or_b32_e32 v98, 10, v220
	v_or_b32_e32 v100, 12, v220
	v_or_b32_e32 v102, 14, v220
	v_or3_b32 v53, v53, v87, v89
	v_or_b32_e32 v87, v86, v220
	v_bitop3_b32 v89, v86, v221, 1 bitop3:0x72
	v_bitop3_b32 v91, v219, v90, v88 bitop3:0x36
	v_bitop3_b32 v90, v86, v90, 1 bitop3:0x36
	v_bitop3_b32 v93, v219, v92, v88 bitop3:0x36
	v_bitop3_b32 v92, v86, v92, 1 bitop3:0x36
	v_bitop3_b32 v95, v219, v94, v88 bitop3:0x36
	v_bitop3_b32 v94, v86, v94, 1 bitop3:0x36
	v_bitop3_b32 v97, v219, v96, v88 bitop3:0x36
	v_bitop3_b32 v96, v86, v96, 1 bitop3:0x36
	v_bitop3_b32 v99, v219, v98, v88 bitop3:0x36
	v_bitop3_b32 v98, v86, v98, 1 bitop3:0x36
	v_bitop3_b32 v101, v219, v100, v88 bitop3:0x36
	v_bitop3_b32 v100, v86, v100, 1 bitop3:0x36
	v_bitop3_b32 v88, v219, v102, v88 bitop3:0x36
	v_bitop3_b32 v86, v86, v102, 1 bitop3:0x36
	v_lshl_or_b32 v87, v87, 4, v53
	v_lshlrev_b32_e32 v89, 4, v89
	v_lshl_or_b32 v91, v91, 4, v53
	v_lshlrev_b32_e32 v90, 4, v90
	v_lshl_or_b32 v93, v93, 4, v53
	v_lshlrev_b32_e32 v92, 4, v92
	v_lshl_or_b32 v95, v95, 4, v53
	v_lshlrev_b32_e32 v94, 4, v94
	v_lshl_or_b32 v97, v97, 4, v53
	v_lshlrev_b32_e32 v96, 4, v96
	v_lshl_or_b32 v99, v99, 4, v53
	v_lshlrev_b32_e32 v98, 4, v98
	v_lshl_or_b32 v101, v101, 4, v53
	v_lshlrev_b32_e32 v100, 4, v100
	v_lshl_or_b32 v88, v88, 4, v53
	v_lshlrev_b32_e32 v86, 4, v86
	s_mov_b64 s[42:43], -1
	s_and_b64 vcc, exec, s[6:7]
	v_add_u32_e32 v218, 0, v87
	v_add3_u32 v217, v89, v53, 0
	v_add_u32_e32 v216, 0, v91
	v_add3_u32 v215, v90, v53, 0
	v_add_u32_e32 v214, 0, v93
	v_add3_u32 v213, v92, v53, 0
	v_add_u32_e32 v212, 0, v95
	v_add3_u32 v211, v94, v53, 0
	v_add_u32_e32 v210, 0, v97
	v_add3_u32 v209, v96, v53, 0
	v_add_u32_e32 v207, 0, v99
	v_add3_u32 v206, v98, v53, 0
	v_add_u32_e32 v205, 0, v101
	v_add3_u32 v204, v100, v53, 0
	v_add_u32_e32 v203, 0, v88
	v_add3_u32 v202, v86, v53, 0
	s_cbranch_vccnz .LBB0_571
	s_waitcnt vmcnt(23)
	v_cvt_pk_bf16_f32 v86, v6, v7
	v_cvt_pk_bf16_f32 v87, v8, v9
	v_cvt_pk_bf16_f32 v88, v2, v3
	v_cvt_pk_bf16_f32 v89, v4, v5
	s_waitcnt vmcnt(21)
	v_cvt_pk_bf16_f32 v154, v14, v15
	v_cvt_pk_bf16_f32 v155, v16, v17
	v_cvt_pk_bf16_f32 v156, v10, v11
	v_cvt_pk_bf16_f32 v157, v12, v13
	s_waitcnt vmcnt(19)
	v_cvt_pk_bf16_f32 v158, v22, v23
	v_cvt_pk_bf16_f32 v159, v24, v25
	v_cvt_pk_bf16_f32 v160, v18, v19
	v_cvt_pk_bf16_f32 v161, v20, v21
	s_waitcnt vmcnt(17)
	v_cvt_pk_bf16_f32 v150, v34, v35
	v_cvt_pk_bf16_f32 v151, v36, v37
	v_cvt_pk_bf16_f32 v152, v30, v31
	v_cvt_pk_bf16_f32 v153, v32, v33
	ds_read_b64_tr_b16 v[90:91], v218
	ds_read_b64_tr_b16 v[92:93], v217 offset:1024
	ds_read_b64_tr_b16 v[94:95], v218 offset:8192
	ds_read_b64_tr_b16 v[96:97], v217 offset:9216
	s_waitcnt lgkmcnt(2)
	v_mfma_f32_16x16x32_bf16 v[90:93], v[90:93], v[86:89], 0
	s_add_i32 s6, s86, 0xffffff80
	s_lshr_b32 s12, s6, 7
	s_add_i32 s6, s46, 0xfffff800
	s_waitcnt lgkmcnt(0)
	v_mfma_f32_16x16x32_bf16 v[90:93], v[94:97], v[154:157], v[90:93]
	ds_read_b64_tr_b16 v[94:95], v218 offset:16384
	ds_read_b64_tr_b16 v[96:97], v217 offset:17408
	s_and_b32 s6, s6, 0x780
	s_lshl_b64 s[30:31], s[12:13], 11
	s_waitcnt lgkmcnt(0)
	v_mfma_f32_16x16x32_bf16 v[90:93], v[94:97], v[158:161], v[90:93]
	ds_read_b64_tr_b16 v[94:95], v218 offset:24576
	ds_read_b64_tr_b16 v[96:97], v217 offset:25600
	s_or_b32 s30, s30, s6
	v_mov_b32_e32 v53, v163
	s_waitcnt lgkmcnt(0)
	v_mfma_f32_16x16x32_bf16 v[146:149], v[94:97], v[150:153], v[90:93]
	s_nop 2
	ds_read_b64_tr_b16 v[90:91], v216
	ds_read_b64_tr_b16 v[92:93], v215 offset:1024
	ds_read_b64_tr_b16 v[94:95], v216 offset:8192
	ds_read_b64_tr_b16 v[96:97], v215 offset:9216
	v_lshl_add_u64 v[52:53], s[30:31], 0, v[52:53]
	s_waitcnt lgkmcnt(2)
	v_mfma_f32_16x16x32_bf16 v[90:93], v[90:93], v[86:89], 0
	v_lshlrev_b64 v[52:53], 12, v[52:53]
	s_and_b32 s6, s47, 0x700
	v_lshl_add_u64 v[52:53], s[10:11], 0, v[52:53]
	s_waitcnt lgkmcnt(0)
	v_mfma_f32_16x16x32_bf16 v[90:93], v[94:97], v[154:157], v[90:93]
	ds_read_b64_tr_b16 v[94:95], v216 offset:16384
	ds_read_b64_tr_b16 v[96:97], v215 offset:17408
	s_lshl_b32 s12, s6, 1
	v_lshl_add_u64 v[52:53], v[52:53], 0, s[12:13]
	s_waitcnt lgkmcnt(0)
	v_mfma_f32_16x16x32_bf16 v[90:93], v[94:97], v[158:161], v[90:93]
	ds_read_b64_tr_b16 v[94:95], v216 offset:24576
	ds_read_b64_tr_b16 v[96:97], v215 offset:25600
	s_cmp_lg_u32 s98, 0
	s_cbranch_scc1 .Lp4w8
	s_waitcnt vmcnt(0)
	s_branch .Lp4wj
.Lp4w8:
	s_waitcnt vmcnt(8)
.Lp4wj:
	v_add_f32_e32 v146, v208, v146
	v_add_f32_e32 v147, v208, v147
	s_waitcnt lgkmcnt(0)
	v_mfma_f32_16x16x32_bf16 v[142:145], v[94:97], v[150:153], v[90:93]
	s_nop 2
	ds_read_b64_tr_b16 v[90:91], v214
	ds_read_b64_tr_b16 v[92:93], v213 offset:1024
	ds_read_b64_tr_b16 v[94:95], v214 offset:8192
	ds_read_b64_tr_b16 v[96:97], v213 offset:9216
	v_add_f32_e32 v148, v208, v148
	s_waitcnt lgkmcnt(2)
	v_mfma_f32_16x16x32_bf16 v[90:93], v[90:93], v[86:89], 0
	v_add_f32_e32 v149, v208, v149
	v_add_f32_e32 v142, v208, v142
	v_add_f32_e32 v143, v208, v143
	s_waitcnt lgkmcnt(0)
	v_mfma_f32_16x16x32_bf16 v[90:93], v[94:97], v[154:157], v[90:93]
	ds_read_b64_tr_b16 v[94:95], v214 offset:16384
	ds_read_b64_tr_b16 v[96:97], v213 offset:17408
	v_add_f32_e32 v144, v208, v144
	v_add_f32_e32 v145, v208, v145
	s_waitcnt lgkmcnt(0)
	v_mfma_f32_16x16x32_bf16 v[90:93], v[94:97], v[158:161], v[90:93]
	ds_read_b64_tr_b16 v[94:95], v214 offset:24576
	ds_read_b64_tr_b16 v[96:97], v213 offset:25600
	s_mov_b64 s[42:43], 0
	s_waitcnt lgkmcnt(0)
	v_mfma_f32_16x16x32_bf16 v[138:141], v[94:97], v[150:153], v[90:93]
	s_nop 2
	ds_read_b64_tr_b16 v[90:91], v212
	ds_read_b64_tr_b16 v[92:93], v211 offset:1024
	ds_read_b64_tr_b16 v[94:95], v212 offset:8192
	ds_read_b64_tr_b16 v[96:97], v211 offset:9216
	s_nop 0
	v_add_f32_e32 v138, v208, v138
	s_waitcnt lgkmcnt(2)
	v_mfma_f32_16x16x32_bf16 v[90:93], v[90:93], v[86:89], 0
	v_add_f32_e32 v139, v208, v139
	v_add_f32_e32 v140, v208, v140
	v_add_f32_e32 v141, v208, v141
	s_waitcnt lgkmcnt(0)
	v_mfma_f32_16x16x32_bf16 v[90:93], v[94:97], v[154:157], v[90:93]
	ds_read_b64_tr_b16 v[94:95], v212 offset:16384
	ds_read_b64_tr_b16 v[96:97], v211 offset:17408
	s_waitcnt lgkmcnt(0)
	v_mfma_f32_16x16x32_bf16 v[90:93], v[94:97], v[158:161], v[90:93]
	ds_read_b64_tr_b16 v[94:95], v212 offset:24576
	ds_read_b64_tr_b16 v[96:97], v211 offset:25600
	s_waitcnt lgkmcnt(0)
	v_mfma_f32_16x16x32_bf16 v[134:137], v[94:97], v[150:153], v[90:93]
	s_nop 3
	ds_read_b64_tr_b16 v[90:91], v210
	ds_read_b64_tr_b16 v[92:93], v209 offset:1024
	ds_read_b64_tr_b16 v[94:95], v210 offset:8192
	ds_read_b64_tr_b16 v[96:97], v209 offset:9216
	v_add_f32_e32 v134, v208, v134
	s_waitcnt lgkmcnt(2)
	v_mfma_f32_16x16x32_bf16 v[90:93], v[90:93], v[86:89], 0
	v_add_f32_e32 v135, v208, v135
	v_add_f32_e32 v136, v208, v136
	v_add_f32_e32 v137, v208, v137
	s_waitcnt lgkmcnt(0)
	v_mfma_f32_16x16x32_bf16 v[90:93], v[94:97], v[154:157], v[90:93]
	ds_read_b64_tr_b16 v[94:95], v210 offset:16384
	ds_read_b64_tr_b16 v[96:97], v209 offset:17408
	s_waitcnt lgkmcnt(0)
	v_mfma_f32_16x16x32_bf16 v[90:93], v[94:97], v[158:161], v[90:93]
	ds_read_b64_tr_b16 v[94:95], v210 offset:24576
	ds_read_b64_tr_b16 v[96:97], v209 offset:25600
	s_waitcnt lgkmcnt(0)
	v_mfma_f32_16x16x32_bf16 v[130:133], v[94:97], v[150:153], v[90:93]
	s_nop 3
	ds_read_b64_tr_b16 v[90:91], v207
	ds_read_b64_tr_b16 v[92:93], v206 offset:1024
	ds_read_b64_tr_b16 v[94:95], v207 offset:8192
	ds_read_b64_tr_b16 v[96:97], v206 offset:9216
	v_add_f32_e32 v130, v208, v130
	s_waitcnt lgkmcnt(2)
	v_mfma_f32_16x16x32_bf16 v[90:93], v[90:93], v[86:89], 0
	v_add_f32_e32 v131, v208, v131
	v_add_f32_e32 v132, v208, v132
	v_add_f32_e32 v133, v208, v133
	s_waitcnt lgkmcnt(0)
	v_mfma_f32_16x16x32_bf16 v[90:93], v[94:97], v[154:157], v[90:93]
	ds_read_b64_tr_b16 v[94:95], v207 offset:16384
	ds_read_b64_tr_b16 v[96:97], v206 offset:17408
	s_waitcnt lgkmcnt(0)
	v_mfma_f32_16x16x32_bf16 v[90:93], v[94:97], v[158:161], v[90:93]
	ds_read_b64_tr_b16 v[94:95], v207 offset:24576
	ds_read_b64_tr_b16 v[96:97], v206 offset:25600
	s_waitcnt lgkmcnt(0)
	v_mfma_f32_16x16x32_bf16 v[126:129], v[94:97], v[150:153], v[90:93]
	s_nop 3
	ds_read_b64_tr_b16 v[90:91], v205
	ds_read_b64_tr_b16 v[92:93], v204 offset:1024
	ds_read_b64_tr_b16 v[94:95], v205 offset:8192
	ds_read_b64_tr_b16 v[96:97], v204 offset:9216
	v_add_f32_e32 v126, v208, v126
	s_waitcnt lgkmcnt(2)
	v_mfma_f32_16x16x32_bf16 v[90:93], v[90:93], v[86:89], 0
	v_add_f32_e32 v127, v208, v127
	v_add_f32_e32 v128, v208, v128
	v_add_f32_e32 v129, v208, v129
	s_waitcnt lgkmcnt(0)
	v_mfma_f32_16x16x32_bf16 v[90:93], v[94:97], v[154:157], v[90:93]
	ds_read_b64_tr_b16 v[94:95], v205 offset:16384
	ds_read_b64_tr_b16 v[96:97], v204 offset:17408
	s_waitcnt lgkmcnt(0)
	v_mfma_f32_16x16x32_bf16 v[90:93], v[94:97], v[158:161], v[90:93]
	ds_read_b64_tr_b16 v[94:95], v205 offset:24576
	ds_read_b64_tr_b16 v[96:97], v204 offset:25600
	s_waitcnt lgkmcnt(0)
	v_mfma_f32_16x16x32_bf16 v[122:125], v[94:97], v[150:153], v[90:93]
	s_nop 3
	ds_read_b64_tr_b16 v[90:91], v203
	ds_read_b64_tr_b16 v[92:93], v202 offset:1024
	ds_read_b64_tr_b16 v[94:95], v203 offset:8192
	ds_read_b64_tr_b16 v[96:97], v202 offset:9216
	v_add_f32_e32 v122, v208, v122
	s_waitcnt lgkmcnt(2)
	v_mfma_f32_16x16x32_bf16 v[90:93], v[90:93], v[86:89], 0
	v_add_f32_e32 v123, v208, v123
	v_add_f32_e32 v124, v208, v124
	v_add_f32_e32 v125, v208, v125
	s_waitcnt lgkmcnt(0)
	v_mfma_f32_16x16x32_bf16 v[90:93], v[94:97], v[154:157], v[90:93]
	ds_read_b64_tr_b16 v[94:95], v203 offset:16384
	ds_read_b64_tr_b16 v[96:97], v202 offset:17408
	s_waitcnt lgkmcnt(0)
	v_mfma_f32_16x16x32_bf16 v[90:93], v[94:97], v[158:161], v[90:93]
	ds_read_b64_tr_b16 v[94:95], v203 offset:24576
	ds_read_b64_tr_b16 v[96:97], v202 offset:25600
	s_waitcnt lgkmcnt(0)
	v_mfma_f32_16x16x32_bf16 v[118:121], v[94:97], v[150:153], v[90:93]
	s_nop 3
	ds_read_b64_tr_b16 v[90:91], v218 offset:32768
	ds_read_b64_tr_b16 v[92:93], v217 offset:33792
	ds_read_b64_tr_b16 v[94:95], v218 offset:40960
	ds_read_b64_tr_b16 v[96:97], v217 offset:41984
	v_add_f32_e32 v118, v208, v118
	s_waitcnt lgkmcnt(2)
	v_mfma_f32_16x16x32_bf16 v[90:93], v[90:93], v[86:89], 0
	v_add_f32_e32 v119, v208, v119
	v_add_f32_e32 v120, v208, v120
	v_add_f32_e32 v121, v208, v121
	s_waitcnt lgkmcnt(0)
	v_mfma_f32_16x16x32_bf16 v[90:93], v[94:97], v[154:157], v[90:93]
	ds_read_b64_tr_b16 v[94:95], v218 offset:49152
	ds_read_b64_tr_b16 v[96:97], v217 offset:50176
	s_waitcnt lgkmcnt(0)
	v_mfma_f32_16x16x32_bf16 v[90:93], v[94:97], v[158:161], v[90:93]
	ds_read_b64_tr_b16 v[94:95], v218 offset:57344
	ds_read_b64_tr_b16 v[96:97], v217 offset:58368
	s_waitcnt lgkmcnt(0)
	v_mfma_f32_16x16x32_bf16 v[114:117], v[94:97], v[150:153], v[90:93]
	s_nop 3
	ds_read_b64_tr_b16 v[90:91], v216 offset:32768
	ds_read_b64_tr_b16 v[92:93], v215 offset:33792
	ds_read_b64_tr_b16 v[94:95], v216 offset:40960
	ds_read_b64_tr_b16 v[96:97], v215 offset:41984
	v_add_f32_e32 v114, v208, v114
	s_waitcnt lgkmcnt(2)
	v_mfma_f32_16x16x32_bf16 v[90:93], v[90:93], v[86:89], 0
	v_add_f32_e32 v115, v208, v115
	v_add_f32_e32 v116, v208, v116
	v_add_f32_e32 v117, v208, v117
	s_waitcnt lgkmcnt(0)
	v_mfma_f32_16x16x32_bf16 v[90:93], v[94:97], v[154:157], v[90:93]
	ds_read_b64_tr_b16 v[94:95], v216 offset:49152
	ds_read_b64_tr_b16 v[96:97], v215 offset:50176
	s_waitcnt lgkmcnt(0)
	v_mfma_f32_16x16x32_bf16 v[90:93], v[94:97], v[158:161], v[90:93]
	ds_read_b64_tr_b16 v[94:95], v216 offset:57344
	ds_read_b64_tr_b16 v[96:97], v215 offset:58368
	s_waitcnt lgkmcnt(0)
	v_mfma_f32_16x16x32_bf16 v[110:113], v[94:97], v[150:153], v[90:93]
	s_nop 3
	ds_read_b64_tr_b16 v[90:91], v214 offset:32768
	ds_read_b64_tr_b16 v[92:93], v213 offset:33792
	ds_read_b64_tr_b16 v[94:95], v214 offset:40960
	ds_read_b64_tr_b16 v[96:97], v213 offset:41984
	v_add_f32_e32 v110, v208, v110
	s_waitcnt lgkmcnt(2)
	v_mfma_f32_16x16x32_bf16 v[90:93], v[90:93], v[86:89], 0
	v_add_f32_e32 v111, v208, v111
	v_add_f32_e32 v112, v208, v112
	v_add_f32_e32 v113, v208, v113
	s_waitcnt lgkmcnt(0)
	v_mfma_f32_16x16x32_bf16 v[90:93], v[94:97], v[154:157], v[90:93]
	ds_read_b64_tr_b16 v[94:95], v214 offset:49152
	ds_read_b64_tr_b16 v[96:97], v213 offset:50176
	s_waitcnt lgkmcnt(0)
	v_mfma_f32_16x16x32_bf16 v[90:93], v[94:97], v[158:161], v[90:93]
	ds_read_b64_tr_b16 v[94:95], v214 offset:57344
	ds_read_b64_tr_b16 v[96:97], v213 offset:58368
	s_waitcnt lgkmcnt(0)
	v_mfma_f32_16x16x32_bf16 v[106:109], v[94:97], v[150:153], v[90:93]
	s_nop 3
	ds_read_b64_tr_b16 v[90:91], v212 offset:32768
	ds_read_b64_tr_b16 v[92:93], v211 offset:33792
	ds_read_b64_tr_b16 v[94:95], v212 offset:40960
	ds_read_b64_tr_b16 v[96:97], v211 offset:41984
	v_add_f32_e32 v106, v208, v106
	s_waitcnt lgkmcnt(2)
	v_mfma_f32_16x16x32_bf16 v[90:93], v[90:93], v[86:89], 0
	v_add_f32_e32 v107, v208, v107
	v_add_f32_e32 v108, v208, v108
	v_add_f32_e32 v109, v208, v109
	s_waitcnt lgkmcnt(0)
	v_mfma_f32_16x16x32_bf16 v[90:93], v[94:97], v[154:157], v[90:93]
	ds_read_b64_tr_b16 v[94:95], v212 offset:49152
	ds_read_b64_tr_b16 v[96:97], v211 offset:50176
	s_waitcnt lgkmcnt(0)
	v_mfma_f32_16x16x32_bf16 v[90:93], v[94:97], v[158:161], v[90:93]
	ds_read_b64_tr_b16 v[94:95], v212 offset:57344
	ds_read_b64_tr_b16 v[96:97], v211 offset:58368
	s_waitcnt lgkmcnt(0)
	v_mfma_f32_16x16x32_bf16 v[102:105], v[94:97], v[150:153], v[90:93]
	s_nop 3
	ds_read_b64_tr_b16 v[90:91], v210 offset:32768
	ds_read_b64_tr_b16 v[92:93], v209 offset:33792
	ds_read_b64_tr_b16 v[94:95], v210 offset:40960
	ds_read_b64_tr_b16 v[96:97], v209 offset:41984
	v_add_f32_e32 v102, v208, v102
	s_waitcnt lgkmcnt(2)
	v_mfma_f32_16x16x32_bf16 v[90:93], v[90:93], v[86:89], 0
	v_add_f32_e32 v103, v208, v103
	v_add_f32_e32 v104, v208, v104
	v_add_f32_e32 v105, v208, v105
	s_waitcnt lgkmcnt(0)
	v_mfma_f32_16x16x32_bf16 v[90:93], v[94:97], v[154:157], v[90:93]
	ds_read_b64_tr_b16 v[94:95], v210 offset:49152
	ds_read_b64_tr_b16 v[96:97], v209 offset:50176
	s_waitcnt lgkmcnt(0)
	v_mfma_f32_16x16x32_bf16 v[90:93], v[94:97], v[158:161], v[90:93]
	ds_read_b64_tr_b16 v[94:95], v210 offset:57344
	ds_read_b64_tr_b16 v[96:97], v209 offset:58368
	s_waitcnt lgkmcnt(0)
	v_mfma_f32_16x16x32_bf16 v[98:101], v[94:97], v[150:153], v[90:93]
	s_nop 3
	ds_read_b64_tr_b16 v[90:91], v207 offset:32768
	ds_read_b64_tr_b16 v[92:93], v206 offset:33792
	ds_read_b64_tr_b16 v[94:95], v207 offset:40960
	ds_read_b64_tr_b16 v[96:97], v206 offset:41984
	v_add_f32_e32 v98, v208, v98
	s_waitcnt lgkmcnt(2)
	v_mfma_f32_16x16x32_bf16 v[90:93], v[90:93], v[86:89], 0
	v_add_f32_e32 v99, v208, v99
	v_add_f32_e32 v100, v208, v100
	v_add_f32_e32 v101, v208, v101
	s_waitcnt lgkmcnt(0)
	v_mfma_f32_16x16x32_bf16 v[90:93], v[94:97], v[154:157], v[90:93]
	ds_read_b64_tr_b16 v[94:95], v207 offset:49152
	ds_read_b64_tr_b16 v[96:97], v206 offset:50176
	s_waitcnt lgkmcnt(0)
	v_mfma_f32_16x16x32_bf16 v[90:93], v[94:97], v[158:161], v[90:93]
	ds_read_b64_tr_b16 v[94:95], v207 offset:57344
	ds_read_b64_tr_b16 v[96:97], v206 offset:58368
	s_waitcnt lgkmcnt(0)
	v_mfma_f32_16x16x32_bf16 v[94:97], v[94:97], v[150:153], v[90:93]
	s_nop 3
	ds_read_b64_tr_b16 v[90:91], v205 offset:32768
	ds_read_b64_tr_b16 v[92:93], v204 offset:33792
	ds_read_b64_tr_b16 v[222:223], v205 offset:40960
	ds_read_b64_tr_b16 v[224:225], v204 offset:41984
	v_add_f32_e32 v94, v208, v94
	s_waitcnt lgkmcnt(2)
	v_mfma_f32_16x16x32_bf16 v[90:93], v[90:93], v[86:89], 0
	v_add_f32_e32 v95, v208, v95
	v_add_f32_e32 v96, v208, v96
	v_add_f32_e32 v97, v208, v97
	s_waitcnt lgkmcnt(0)
	v_mfma_f32_16x16x32_bf16 v[90:93], v[222:225], v[154:157], v[90:93]
	ds_read_b64_tr_b16 v[222:223], v205 offset:49152
	ds_read_b64_tr_b16 v[224:225], v204 offset:50176
	s_waitcnt lgkmcnt(0)
	v_mfma_f32_16x16x32_bf16 v[90:93], v[222:225], v[158:161], v[90:93]
	ds_read_b64_tr_b16 v[222:223], v205 offset:57344
	ds_read_b64_tr_b16 v[224:225], v204 offset:58368
	s_waitcnt lgkmcnt(0)
	v_mfma_f32_16x16x32_bf16 v[90:93], v[222:225], v[150:153], v[90:93]
	ds_read_b64_tr_b16 v[222:223], v203 offset:32768
	ds_read_b64_tr_b16 v[224:225], v202 offset:33792
	s_waitcnt lgkmcnt(0)
	v_mfma_f32_16x16x32_bf16 v[86:89], v[222:225], v[86:89], 0
	ds_read_b64_tr_b16 v[222:223], v203 offset:40960
	ds_read_b64_tr_b16 v[224:225], v202 offset:41984
	s_nop 1
	v_add_f32_e32 v90, v208, v90
	v_add_f32_e32 v91, v208, v91
	s_waitcnt lgkmcnt(0)
	v_mfma_f32_16x16x32_bf16 v[86:89], v[222:225], v[154:157], v[86:89]
	ds_read_b64_tr_b16 v[154:155], v203 offset:49152
	ds_read_b64_tr_b16 v[156:157], v202 offset:50176
	v_add_f32_e32 v92, v208, v92
	v_add_f32_e32 v93, v208, v93
	s_waitcnt lgkmcnt(0)
	v_mfma_f32_16x16x32_bf16 v[86:89], v[154:157], v[158:161], v[86:89]
	ds_read_b64_tr_b16 v[154:155], v203 offset:57344
	ds_read_b64_tr_b16 v[156:157], v202 offset:58368
	s_waitcnt lgkmcnt(0)
	v_mfma_f32_16x16x32_bf16 v[86:89], v[154:157], v[150:153], v[86:89]
	v_and_b32_e32 v150, 16, v221
	v_mov_b32_e32 v151, v163
	v_lshl_add_u64 v[52:53], v[52:53], 0, v[150:151]
	v_lshlrev_b32_e32 v150, 16, v194
	v_mul_f32_e32 v151, 0x3d372713, v150
	v_mul_f32_e32 v151, v151, v150
	v_fma_f32 v151, v151, v150, v150
	v_mul_f32_e32 v151, 0x3f4c422a, v151
	v_mul_f32_e32 v151, -2.0, v151
	v_mul_f32_e32 v151, 0x3fb8aa3b, v151
	v_exp_f32_e32 v151, v151
	v_and_b32_e32 v152, 16, v201
	v_add_f32_e32 v86, v208, v86
	v_add_f32_e32 v87, v208, v87
	v_add_f32_e32 v151, 1.0, v151
	v_rcp_f32_e32 v151, v151
	v_add_f32_e32 v88, v208, v88
	v_add_f32_e32 v89, v208, v89
	v_mul_f32_e32 v150, v151, v150
	v_mul_f32_e32 v146, v150, v146
	v_and_b32_e32 v150, 0xffff0000, v194
	v_mul_f32_e32 v151, 0x3d372713, v150
	v_mul_f32_e32 v151, v151, v150
	v_fma_f32 v151, v151, v150, v150
	v_mul_f32_e32 v151, 0x3f4c422a, v151
	v_mul_f32_e32 v151, -2.0, v151
	v_mul_f32_e32 v151, 0x3fb8aa3b, v151
	v_exp_f32_e32 v151, v151
	s_nop 0
	v_add_f32_e32 v151, 1.0, v151
	v_rcp_f32_e32 v151, v151
	s_nop 0
	v_mul_f32_e32 v150, v151, v150
	v_mul_f32_e32 v147, v150, v147
	v_lshlrev_b32_e32 v150, 16, v195
	v_mul_f32_e32 v151, 0x3d372713, v150
	v_mul_f32_e32 v151, v151, v150
	v_fma_f32 v151, v151, v150, v150
	v_mul_f32_e32 v151, 0x3f4c422a, v151
	v_mul_f32_e32 v151, -2.0, v151
	v_mul_f32_e32 v151, 0x3fb8aa3b, v151
	v_exp_f32_e32 v151, v151
	v_cvt_pk_bf16_f32 v146, v146, v147
	s_nop 0
	v_add_f32_e32 v151, 1.0, v151
	v_rcp_f32_e32 v151, v151
	s_nop 0
	v_mul_f32_e32 v150, v151, v150
	v_mul_f32_e32 v148, v150, v148
	v_and_b32_e32 v150, 0xffff0000, v195
	v_mul_f32_e32 v151, 0x3d372713, v150
	v_mul_f32_e32 v151, v151, v150
	v_fma_f32 v151, v151, v150, v150
	v_mul_f32_e32 v151, 0x3f4c422a, v151
	v_mul_f32_e32 v151, -2.0, v151
	v_mul_f32_e32 v151, 0x3fb8aa3b, v151
	v_exp_f32_e32 v151, v151
	s_nop 0
	v_add_f32_e32 v151, 1.0, v151
	v_rcp_f32_e32 v151, v151
	s_nop 0
	v_mul_f32_e32 v150, v151, v150
	v_mul_f32_e32 v149, v150, v149
	v_cvt_pk_bf16_f32 v147, v148, v149
	v_lshlrev_b32_e32 v148, 16, v186
	v_mul_f32_e32 v149, 0x3d372713, v148
	v_mul_f32_e32 v149, v149, v148
	v_fma_f32 v149, v149, v148, v148
	v_mul_f32_e32 v149, 0x3f4c422a, v149
	v_mul_f32_e32 v149, -2.0, v149
	v_mul_f32_e32 v149, 0x3fb8aa3b, v149
	v_exp_f32_e32 v149, v149
	s_nop 0
	v_add_f32_e32 v149, 1.0, v149
	v_rcp_f32_e32 v149, v149
	s_nop 0
	v_mul_f32_e32 v148, v149, v148
	v_mul_f32_e32 v142, v148, v142
	v_and_b32_e32 v148, 0xffff0000, v186
	v_mul_f32_e32 v149, 0x3d372713, v148
	v_mul_f32_e32 v149, v149, v148
	v_fma_f32 v149, v149, v148, v148
	v_mul_f32_e32 v149, 0x3f4c422a, v149
	v_mul_f32_e32 v149, -2.0, v149
	v_mul_f32_e32 v149, 0x3fb8aa3b, v149
	v_exp_f32_e32 v149, v149
	s_nop 0
	v_add_f32_e32 v149, 1.0, v149
	v_rcp_f32_e32 v149, v149
	s_nop 0
	v_mul_f32_e32 v148, v149, v148
	v_mul_f32_e32 v143, v148, v143
	v_lshlrev_b32_e32 v148, 16, v187
	v_mul_f32_e32 v149, 0x3d372713, v148
	v_mul_f32_e32 v149, v149, v148
	v_fma_f32 v149, v149, v148, v148
	v_mul_f32_e32 v149, 0x3f4c422a, v149
	v_mul_f32_e32 v149, -2.0, v149
	v_mul_f32_e32 v149, 0x3fb8aa3b, v149
	v_exp_f32_e32 v149, v149
	s_nop 0
	v_add_f32_e32 v149, 1.0, v149
	v_rcp_f32_e32 v149, v149
	s_nop 0
	v_mul_f32_e32 v148, v149, v148
	v_mul_f32_e32 v144, v148, v144
	v_and_b32_e32 v148, 0xffff0000, v187
	v_mul_f32_e32 v149, 0x3d372713, v148
	v_mul_f32_e32 v149, v149, v148
	v_fma_f32 v149, v149, v148, v148
	v_mul_f32_e32 v149, 0x3f4c422a, v149
	v_mul_f32_e32 v149, -2.0, v149
	v_mul_f32_e32 v149, 0x3fb8aa3b, v149
	v_exp_f32_e32 v149, v149
	s_nop 0
	v_add_f32_e32 v149, 1.0, v149
	v_rcp_f32_e32 v149, v149
	s_nop 0
	v_mul_f32_e32 v148, v149, v148
	v_mul_f32_e32 v145, v148, v145
	v_cvt_pk_bf16_f32 v148, v142, v143
	v_lshlrev_b32_e32 v142, 1, v152
	v_mov_b32_e32 v143, v163
	v_lshl_add_u64 v[52:53], v[52:53], 0, v[142:143]
	v_lshlrev_b32_e32 v142, 16, v184
	v_mul_f32_e32 v143, 0x3d372713, v142
	v_mul_f32_e32 v143, v143, v142
	v_fma_f32 v143, v143, v142, v142
	v_mul_f32_e32 v143, 0x3f4c422a, v143
	v_mul_f32_e32 v143, -2.0, v143
	v_mul_f32_e32 v143, 0x3fb8aa3b, v143
	v_exp_f32_e32 v143, v143
	v_cvt_pk_bf16_f32 v149, v144, v145
	v_permlane16_swap_b32_e32 v146, v148
	v_add_f32_e32 v143, 1.0, v143
	v_rcp_f32_e32 v143, v143
	v_permlane16_swap_b32_e32 v147, v149
	global_store_dwordx4 v[52:53], v[146:149], off
	v_mul_f32_e32 v142, v143, v142
	v_mul_f32_e32 v138, v142, v138
	v_and_b32_e32 v142, 0xffff0000, v184
	v_mul_f32_e32 v143, 0x3d372713, v142
	v_mul_f32_e32 v143, v143, v142
	v_fma_f32 v143, v143, v142, v142
	v_mul_f32_e32 v143, 0x3f4c422a, v143
	v_mul_f32_e32 v143, -2.0, v143
	v_mul_f32_e32 v143, 0x3fb8aa3b, v143
	v_exp_f32_e32 v143, v143
	s_nop 0
	v_add_f32_e32 v143, 1.0, v143
	v_rcp_f32_e32 v143, v143
	s_nop 0
	v_mul_f32_e32 v142, v143, v142
	v_mul_f32_e32 v139, v142, v139
	v_lshlrev_b32_e32 v142, 16, v185
	v_mul_f32_e32 v143, 0x3d372713, v142
	v_mul_f32_e32 v143, v143, v142
	v_fma_f32 v143, v143, v142, v142
	v_mul_f32_e32 v143, 0x3f4c422a, v143
	v_mul_f32_e32 v143, -2.0, v143
	v_mul_f32_e32 v143, 0x3fb8aa3b, v143
	v_exp_f32_e32 v143, v143
	v_cvt_pk_bf16_f32 v138, v138, v139
	s_nop 0
	v_add_f32_e32 v143, 1.0, v143
	v_rcp_f32_e32 v143, v143
	s_nop 0
	v_mul_f32_e32 v142, v143, v142
	v_mul_f32_e32 v140, v142, v140
	v_and_b32_e32 v142, 0xffff0000, v185
	v_mul_f32_e32 v143, 0x3d372713, v142
	v_mul_f32_e32 v143, v143, v142
	v_fma_f32 v143, v143, v142, v142
	v_mul_f32_e32 v143, 0x3f4c422a, v143
	v_mul_f32_e32 v143, -2.0, v143
	v_mul_f32_e32 v143, 0x3fb8aa3b, v143
	v_exp_f32_e32 v143, v143
	s_nop 0
	v_add_f32_e32 v143, 1.0, v143
	v_rcp_f32_e32 v143, v143
	s_nop 0
	v_mul_f32_e32 v142, v143, v142
	v_mul_f32_e32 v141, v142, v141
	v_cvt_pk_bf16_f32 v139, v140, v141
	v_lshlrev_b32_e32 v140, 16, v182
	v_mul_f32_e32 v141, 0x3d372713, v140
	v_mul_f32_e32 v141, v141, v140
	v_fma_f32 v141, v141, v140, v140
	v_mul_f32_e32 v141, 0x3f4c422a, v141
	v_mul_f32_e32 v141, -2.0, v141
	v_mul_f32_e32 v141, 0x3fb8aa3b, v141
	v_exp_f32_e32 v141, v141
	s_nop 0
	v_add_f32_e32 v141, 1.0, v141
	v_rcp_f32_e32 v141, v141
	s_nop 0
	v_mul_f32_e32 v140, v141, v140
	v_mul_f32_e32 v134, v140, v134
	v_and_b32_e32 v140, 0xffff0000, v182
	v_mul_f32_e32 v141, 0x3d372713, v140
	v_mul_f32_e32 v141, v141, v140
	v_fma_f32 v141, v141, v140, v140
	v_mul_f32_e32 v141, 0x3f4c422a, v141
	v_mul_f32_e32 v141, -2.0, v141
	v_mul_f32_e32 v141, 0x3fb8aa3b, v141
	v_exp_f32_e32 v141, v141
	s_nop 0
	v_add_f32_e32 v141, 1.0, v141
	v_rcp_f32_e32 v141, v141
	s_nop 0
	v_mul_f32_e32 v140, v141, v140
	v_mul_f32_e32 v135, v140, v135
	v_lshlrev_b32_e32 v140, 16, v183
	v_mul_f32_e32 v141, 0x3d372713, v140
	v_mul_f32_e32 v141, v141, v140
	v_fma_f32 v141, v141, v140, v140
	v_mul_f32_e32 v141, 0x3f4c422a, v141
	v_mul_f32_e32 v141, -2.0, v141
	v_mul_f32_e32 v141, 0x3fb8aa3b, v141
	v_exp_f32_e32 v141, v141
	s_nop 0
	v_add_f32_e32 v141, 1.0, v141
	v_rcp_f32_e32 v141, v141
	s_nop 0
	v_mul_f32_e32 v140, v141, v140
	v_mul_f32_e32 v136, v140, v136
	v_and_b32_e32 v140, 0xffff0000, v183
	v_mul_f32_e32 v141, 0x3d372713, v140
	v_mul_f32_e32 v141, v141, v140
	v_fma_f32 v141, v141, v140, v140
	v_mul_f32_e32 v141, 0x3f4c422a, v141
	v_mul_f32_e32 v141, -2.0, v141
	v_mul_f32_e32 v141, 0x3fb8aa3b, v141
	v_exp_f32_e32 v141, v141
	s_nop 0
	v_add_f32_e32 v141, 1.0, v141
	v_rcp_f32_e32 v141, v141
	s_nop 0
	v_mul_f32_e32 v140, v141, v140
	v_mul_f32_e32 v137, v140, v137
	v_cvt_pk_bf16_f32 v140, v134, v135
	v_lshlrev_b32_e32 v134, 16, v180
	v_mul_f32_e32 v135, 0x3d372713, v134
	v_mul_f32_e32 v135, v135, v134
	v_fma_f32 v135, v135, v134, v134
	v_mul_f32_e32 v135, 0x3f4c422a, v135
	v_mul_f32_e32 v135, -2.0, v135
	v_mul_f32_e32 v135, 0x3fb8aa3b, v135
	v_exp_f32_e32 v135, v135
	v_cvt_pk_bf16_f32 v141, v136, v137
	v_permlane16_swap_b32_e32 v138, v140
	v_add_f32_e32 v135, 1.0, v135
	v_rcp_f32_e32 v135, v135
	v_permlane16_swap_b32_e32 v139, v141
	global_store_dwordx4 v[52:53], v[138:141], off offset:64
	v_mul_f32_e32 v134, v135, v134
	v_mul_f32_e32 v130, v134, v130
	v_and_b32_e32 v134, 0xffff0000, v180
	v_mul_f32_e32 v135, 0x3d372713, v134
	v_mul_f32_e32 v135, v135, v134
	v_fma_f32 v135, v135, v134, v134
	v_mul_f32_e32 v135, 0x3f4c422a, v135
	v_mul_f32_e32 v135, -2.0, v135
	v_mul_f32_e32 v135, 0x3fb8aa3b, v135
	v_exp_f32_e32 v135, v135
	s_nop 0
	v_add_f32_e32 v135, 1.0, v135
	v_rcp_f32_e32 v135, v135
	s_nop 0
	v_mul_f32_e32 v134, v135, v134
	v_mul_f32_e32 v131, v134, v131
	v_lshlrev_b32_e32 v134, 16, v181
	v_mul_f32_e32 v135, 0x3d372713, v134
	v_mul_f32_e32 v135, v135, v134
	v_fma_f32 v135, v135, v134, v134
	v_mul_f32_e32 v135, 0x3f4c422a, v135
	v_mul_f32_e32 v135, -2.0, v135
	v_mul_f32_e32 v135, 0x3fb8aa3b, v135
	v_exp_f32_e32 v135, v135
	v_cvt_pk_bf16_f32 v130, v130, v131
	s_nop 0
	v_add_f32_e32 v135, 1.0, v135
	v_rcp_f32_e32 v135, v135
	s_nop 0
	v_mul_f32_e32 v134, v135, v134
	v_mul_f32_e32 v132, v134, v132
	v_and_b32_e32 v134, 0xffff0000, v181
	v_mul_f32_e32 v135, 0x3d372713, v134
	v_mul_f32_e32 v135, v135, v134
	v_fma_f32 v135, v135, v134, v134
	v_mul_f32_e32 v135, 0x3f4c422a, v135
	v_mul_f32_e32 v135, -2.0, v135
	v_mul_f32_e32 v135, 0x3fb8aa3b, v135
	v_exp_f32_e32 v135, v135
	s_nop 0
	v_add_f32_e32 v135, 1.0, v135
	v_rcp_f32_e32 v135, v135
	s_nop 0
	v_mul_f32_e32 v134, v135, v134
	v_mul_f32_e32 v133, v134, v133
	v_cvt_pk_bf16_f32 v131, v132, v133
	v_lshlrev_b32_e32 v132, 16, v178
	v_mul_f32_e32 v133, 0x3d372713, v132
	v_mul_f32_e32 v133, v133, v132
	v_fma_f32 v133, v133, v132, v132
	v_mul_f32_e32 v133, 0x3f4c422a, v133
	v_mul_f32_e32 v133, -2.0, v133
	v_mul_f32_e32 v133, 0x3fb8aa3b, v133
	v_exp_f32_e32 v133, v133
	s_nop 0
	v_add_f32_e32 v133, 1.0, v133
	v_rcp_f32_e32 v133, v133
	s_nop 0
	v_mul_f32_e32 v132, v133, v132
	v_mul_f32_e32 v126, v132, v126
	v_and_b32_e32 v132, 0xffff0000, v178
	v_mul_f32_e32 v133, 0x3d372713, v132
	v_mul_f32_e32 v133, v133, v132
	v_fma_f32 v133, v133, v132, v132
	v_mul_f32_e32 v133, 0x3f4c422a, v133
	v_mul_f32_e32 v133, -2.0, v133
	v_mul_f32_e32 v133, 0x3fb8aa3b, v133
	v_exp_f32_e32 v133, v133
	s_nop 0
	v_add_f32_e32 v133, 1.0, v133
	v_rcp_f32_e32 v133, v133
	s_nop 0
	v_mul_f32_e32 v132, v133, v132
	v_mul_f32_e32 v127, v132, v127
	v_lshlrev_b32_e32 v132, 16, v179
	v_mul_f32_e32 v133, 0x3d372713, v132
	v_mul_f32_e32 v133, v133, v132
	v_fma_f32 v133, v133, v132, v132
	v_mul_f32_e32 v133, 0x3f4c422a, v133
	v_mul_f32_e32 v133, -2.0, v133
	v_mul_f32_e32 v133, 0x3fb8aa3b, v133
	v_exp_f32_e32 v133, v133
	s_nop 0
	v_add_f32_e32 v133, 1.0, v133
	v_rcp_f32_e32 v133, v133
	s_nop 0
	v_mul_f32_e32 v132, v133, v132
	v_mul_f32_e32 v128, v132, v128
	v_and_b32_e32 v132, 0xffff0000, v179
	v_mul_f32_e32 v133, 0x3d372713, v132
	v_mul_f32_e32 v133, v133, v132
	v_fma_f32 v133, v133, v132, v132
	v_mul_f32_e32 v133, 0x3f4c422a, v133
	v_mul_f32_e32 v133, -2.0, v133
	v_mul_f32_e32 v133, 0x3fb8aa3b, v133
	v_exp_f32_e32 v133, v133
	s_nop 0
	v_add_f32_e32 v133, 1.0, v133
	v_rcp_f32_e32 v133, v133
	s_nop 0
	v_mul_f32_e32 v132, v133, v132
	v_mul_f32_e32 v129, v132, v129
	v_cvt_pk_bf16_f32 v132, v126, v127
	v_lshlrev_b32_e32 v126, 16, v176
	v_mul_f32_e32 v127, 0x3d372713, v126
	v_mul_f32_e32 v127, v127, v126
	v_fma_f32 v127, v127, v126, v126
	v_mul_f32_e32 v127, 0x3f4c422a, v127
	v_mul_f32_e32 v127, -2.0, v127
	v_mul_f32_e32 v127, 0x3fb8aa3b, v127
	v_exp_f32_e32 v127, v127
	v_cvt_pk_bf16_f32 v133, v128, v129
	v_permlane16_swap_b32_e32 v130, v132
	v_add_f32_e32 v127, 1.0, v127
	v_rcp_f32_e32 v127, v127
	v_permlane16_swap_b32_e32 v131, v133
	global_store_dwordx4 v[52:53], v[130:133], off offset:128
	v_mul_f32_e32 v126, v127, v126
	v_mul_f32_e32 v122, v126, v122
	v_and_b32_e32 v126, 0xffff0000, v176
	v_mul_f32_e32 v127, 0x3d372713, v126
	v_mul_f32_e32 v127, v127, v126
	v_fma_f32 v127, v127, v126, v126
	v_mul_f32_e32 v127, 0x3f4c422a, v127
	v_mul_f32_e32 v127, -2.0, v127
	v_mul_f32_e32 v127, 0x3fb8aa3b, v127
	v_exp_f32_e32 v127, v127
	s_nop 0
	v_add_f32_e32 v127, 1.0, v127
	v_rcp_f32_e32 v127, v127
	s_nop 0
	v_mul_f32_e32 v126, v127, v126
	v_mul_f32_e32 v123, v126, v123
	v_lshlrev_b32_e32 v126, 16, v177
	v_mul_f32_e32 v127, 0x3d372713, v126
	v_mul_f32_e32 v127, v127, v126
	v_fma_f32 v127, v127, v126, v126
	v_mul_f32_e32 v127, 0x3f4c422a, v127
	v_mul_f32_e32 v127, -2.0, v127
	v_mul_f32_e32 v127, 0x3fb8aa3b, v127
	v_exp_f32_e32 v127, v127
	v_cvt_pk_bf16_f32 v122, v122, v123
	s_nop 0
	v_add_f32_e32 v127, 1.0, v127
	v_rcp_f32_e32 v127, v127
	s_nop 0
	v_mul_f32_e32 v126, v127, v126
	v_mul_f32_e32 v124, v126, v124
	v_and_b32_e32 v126, 0xffff0000, v177
	v_mul_f32_e32 v127, 0x3d372713, v126
	v_mul_f32_e32 v127, v127, v126
	v_fma_f32 v127, v127, v126, v126
	v_mul_f32_e32 v127, 0x3f4c422a, v127
	v_mul_f32_e32 v127, -2.0, v127
	v_mul_f32_e32 v127, 0x3fb8aa3b, v127
	v_exp_f32_e32 v127, v127
	s_nop 0
	v_add_f32_e32 v127, 1.0, v127
	v_rcp_f32_e32 v127, v127
	s_nop 0
	v_mul_f32_e32 v126, v127, v126
	v_mul_f32_e32 v125, v126, v125
	v_cvt_pk_bf16_f32 v123, v124, v125
	v_lshlrev_b32_e32 v124, 16, v174
	v_mul_f32_e32 v125, 0x3d372713, v124
	v_mul_f32_e32 v125, v125, v124
	v_fma_f32 v125, v125, v124, v124
	v_mul_f32_e32 v125, 0x3f4c422a, v125
	v_mul_f32_e32 v125, -2.0, v125
	v_mul_f32_e32 v125, 0x3fb8aa3b, v125
	v_exp_f32_e32 v125, v125
	s_nop 0
	v_add_f32_e32 v125, 1.0, v125
	v_rcp_f32_e32 v125, v125
	s_nop 0
	v_mul_f32_e32 v124, v125, v124
	v_mul_f32_e32 v118, v124, v118
	v_and_b32_e32 v124, 0xffff0000, v174
	v_mul_f32_e32 v125, 0x3d372713, v124
	v_mul_f32_e32 v125, v125, v124
	v_fma_f32 v125, v125, v124, v124
	v_mul_f32_e32 v125, 0x3f4c422a, v125
	v_mul_f32_e32 v125, -2.0, v125
	v_mul_f32_e32 v125, 0x3fb8aa3b, v125
	v_exp_f32_e32 v125, v125
	s_nop 0
	v_add_f32_e32 v125, 1.0, v125
	v_rcp_f32_e32 v125, v125
	s_nop 0
	v_mul_f32_e32 v124, v125, v124
	v_mul_f32_e32 v119, v124, v119
	v_lshlrev_b32_e32 v124, 16, v175
	v_mul_f32_e32 v125, 0x3d372713, v124
	v_mul_f32_e32 v125, v125, v124
	v_fma_f32 v125, v125, v124, v124
	v_mul_f32_e32 v125, 0x3f4c422a, v125
	v_mul_f32_e32 v125, -2.0, v125
	v_mul_f32_e32 v125, 0x3fb8aa3b, v125
	v_exp_f32_e32 v125, v125
	s_nop 0
	v_add_f32_e32 v125, 1.0, v125
	v_rcp_f32_e32 v125, v125
	s_nop 0
	v_mul_f32_e32 v124, v125, v124
	v_mul_f32_e32 v120, v124, v120
	v_and_b32_e32 v124, 0xffff0000, v175
	v_mul_f32_e32 v125, 0x3d372713, v124
	v_mul_f32_e32 v125, v125, v124
	v_fma_f32 v125, v125, v124, v124
	v_mul_f32_e32 v125, 0x3f4c422a, v125
	v_mul_f32_e32 v125, -2.0, v125
	v_mul_f32_e32 v125, 0x3fb8aa3b, v125
	v_exp_f32_e32 v125, v125
	s_nop 0
	v_add_f32_e32 v125, 1.0, v125
	v_rcp_f32_e32 v125, v125
	s_nop 0
	v_mul_f32_e32 v124, v125, v124
	v_mul_f32_e32 v121, v124, v121
	v_cvt_pk_bf16_f32 v124, v118, v119
	v_lshlrev_b32_e32 v118, 16, v172
	v_mul_f32_e32 v119, 0x3d372713, v118
	v_mul_f32_e32 v119, v119, v118
	v_fma_f32 v119, v119, v118, v118
	v_mul_f32_e32 v119, 0x3f4c422a, v119
	v_mul_f32_e32 v119, -2.0, v119
	v_mul_f32_e32 v119, 0x3fb8aa3b, v119
	v_exp_f32_e32 v119, v119
	v_cvt_pk_bf16_f32 v125, v120, v121
	v_permlane16_swap_b32_e32 v122, v124
	v_add_f32_e32 v119, 1.0, v119
	v_rcp_f32_e32 v119, v119
	v_permlane16_swap_b32_e32 v123, v125
	global_store_dwordx4 v[52:53], v[122:125], off offset:192
	v_mul_f32_e32 v118, v119, v118
	v_mul_f32_e32 v114, v118, v114
	v_and_b32_e32 v118, 0xffff0000, v172
	v_mul_f32_e32 v119, 0x3d372713, v118
	v_mul_f32_e32 v119, v119, v118
	v_fma_f32 v119, v119, v118, v118
	v_mul_f32_e32 v119, 0x3f4c422a, v119
	v_mul_f32_e32 v119, -2.0, v119
	v_mul_f32_e32 v119, 0x3fb8aa3b, v119
	v_exp_f32_e32 v119, v119
	s_nop 0
	v_add_f32_e32 v119, 1.0, v119
	v_rcp_f32_e32 v119, v119
	s_nop 0
	v_mul_f32_e32 v118, v119, v118
	v_mul_f32_e32 v115, v118, v115
	v_lshlrev_b32_e32 v118, 16, v173
	v_mul_f32_e32 v119, 0x3d372713, v118
	v_mul_f32_e32 v119, v119, v118
	v_fma_f32 v119, v119, v118, v118
	v_mul_f32_e32 v119, 0x3f4c422a, v119
	v_mul_f32_e32 v119, -2.0, v119
	v_mul_f32_e32 v119, 0x3fb8aa3b, v119
	v_exp_f32_e32 v119, v119
	v_cvt_pk_bf16_f32 v114, v114, v115
	s_nop 0
	v_add_f32_e32 v119, 1.0, v119
	v_rcp_f32_e32 v119, v119
	s_nop 0
	v_mul_f32_e32 v118, v119, v118
	v_mul_f32_e32 v116, v118, v116
	v_and_b32_e32 v118, 0xffff0000, v173
	v_mul_f32_e32 v119, 0x3d372713, v118
	v_mul_f32_e32 v119, v119, v118
	v_fma_f32 v119, v119, v118, v118
	v_mul_f32_e32 v119, 0x3f4c422a, v119
	v_mul_f32_e32 v119, -2.0, v119
	v_mul_f32_e32 v119, 0x3fb8aa3b, v119
	v_exp_f32_e32 v119, v119
	s_nop 0
	v_add_f32_e32 v119, 1.0, v119
	v_rcp_f32_e32 v119, v119
	s_nop 0
	v_mul_f32_e32 v118, v119, v118
	v_mul_f32_e32 v117, v118, v117
	v_cvt_pk_bf16_f32 v115, v116, v117
	v_lshlrev_b32_e32 v116, 16, v170
	v_mul_f32_e32 v117, 0x3d372713, v116
	v_mul_f32_e32 v117, v117, v116
	v_fma_f32 v117, v117, v116, v116
	v_mul_f32_e32 v117, 0x3f4c422a, v117
	v_mul_f32_e32 v117, -2.0, v117
	v_mul_f32_e32 v117, 0x3fb8aa3b, v117
	v_exp_f32_e32 v117, v117
	s_nop 0
	v_add_f32_e32 v117, 1.0, v117
	v_rcp_f32_e32 v117, v117
	s_nop 0
	v_mul_f32_e32 v116, v117, v116
	v_mul_f32_e32 v110, v116, v110
	v_and_b32_e32 v116, 0xffff0000, v170
	v_mul_f32_e32 v117, 0x3d372713, v116
	v_mul_f32_e32 v117, v117, v116
	v_fma_f32 v117, v117, v116, v116
	v_mul_f32_e32 v117, 0x3f4c422a, v117
	v_mul_f32_e32 v117, -2.0, v117
	v_mul_f32_e32 v117, 0x3fb8aa3b, v117
	v_exp_f32_e32 v117, v117
	s_nop 0
	v_add_f32_e32 v117, 1.0, v117
	v_rcp_f32_e32 v117, v117
	s_nop 0
	v_mul_f32_e32 v116, v117, v116
	v_mul_f32_e32 v111, v116, v111
	v_lshlrev_b32_e32 v116, 16, v171
	v_mul_f32_e32 v117, 0x3d372713, v116
	v_mul_f32_e32 v117, v117, v116
	v_fma_f32 v117, v117, v116, v116
	v_mul_f32_e32 v117, 0x3f4c422a, v117
	v_mul_f32_e32 v117, -2.0, v117
	v_mul_f32_e32 v117, 0x3fb8aa3b, v117
	v_exp_f32_e32 v117, v117
	s_nop 0
	v_add_f32_e32 v117, 1.0, v117
	v_rcp_f32_e32 v117, v117
	s_nop 0
	v_mul_f32_e32 v116, v117, v116
	v_mul_f32_e32 v112, v116, v112
	v_and_b32_e32 v116, 0xffff0000, v171
	v_mul_f32_e32 v117, 0x3d372713, v116
	v_mul_f32_e32 v117, v117, v116
	v_fma_f32 v117, v117, v116, v116
	v_mul_f32_e32 v117, 0x3f4c422a, v117
	v_mul_f32_e32 v117, -2.0, v117
	v_mul_f32_e32 v117, 0x3fb8aa3b, v117
	v_exp_f32_e32 v117, v117
	s_nop 0
	v_add_f32_e32 v117, 1.0, v117
	v_rcp_f32_e32 v117, v117
	s_nop 0
	v_mul_f32_e32 v116, v117, v116
	v_mul_f32_e32 v113, v116, v113
	v_cvt_pk_bf16_f32 v116, v110, v111
	v_lshlrev_b32_e32 v110, 16, v168
	v_mul_f32_e32 v111, 0x3d372713, v110
	v_mul_f32_e32 v111, v111, v110
	v_fma_f32 v111, v111, v110, v110
	v_mul_f32_e32 v111, 0x3f4c422a, v111
	v_mul_f32_e32 v111, -2.0, v111
	v_mul_f32_e32 v111, 0x3fb8aa3b, v111
	v_exp_f32_e32 v111, v111
	v_cvt_pk_bf16_f32 v117, v112, v113
	v_permlane16_swap_b32_e32 v114, v116
	v_add_f32_e32 v111, 1.0, v111
	v_rcp_f32_e32 v111, v111
	v_permlane16_swap_b32_e32 v115, v117
	global_store_dwordx4 v[52:53], v[114:117], off offset:256
	v_mul_f32_e32 v110, v111, v110
	v_mul_f32_e32 v106, v110, v106
	v_and_b32_e32 v110, 0xffff0000, v168
	v_mul_f32_e32 v111, 0x3d372713, v110
	v_mul_f32_e32 v111, v111, v110
	v_fma_f32 v111, v111, v110, v110
	v_mul_f32_e32 v111, 0x3f4c422a, v111
	v_mul_f32_e32 v111, -2.0, v111
	v_mul_f32_e32 v111, 0x3fb8aa3b, v111
	v_exp_f32_e32 v111, v111
	s_nop 0
	v_add_f32_e32 v111, 1.0, v111
	v_rcp_f32_e32 v111, v111
	s_nop 0
	v_mul_f32_e32 v110, v111, v110
	v_mul_f32_e32 v107, v110, v107
	v_lshlrev_b32_e32 v110, 16, v169
	v_mul_f32_e32 v111, 0x3d372713, v110
	v_mul_f32_e32 v111, v111, v110
	v_fma_f32 v111, v111, v110, v110
	v_mul_f32_e32 v111, 0x3f4c422a, v111
	v_mul_f32_e32 v111, -2.0, v111
	v_mul_f32_e32 v111, 0x3fb8aa3b, v111
	v_exp_f32_e32 v111, v111
	v_cvt_pk_bf16_f32 v106, v106, v107
	s_nop 0
	v_add_f32_e32 v111, 1.0, v111
	v_rcp_f32_e32 v111, v111
	s_nop 0
	v_mul_f32_e32 v110, v111, v110
	v_mul_f32_e32 v108, v110, v108
	v_and_b32_e32 v110, 0xffff0000, v169
	v_mul_f32_e32 v111, 0x3d372713, v110
	v_mul_f32_e32 v111, v111, v110
	v_fma_f32 v111, v111, v110, v110
	v_mul_f32_e32 v111, 0x3f4c422a, v111
	v_mul_f32_e32 v111, -2.0, v111
	v_mul_f32_e32 v111, 0x3fb8aa3b, v111
	v_exp_f32_e32 v111, v111
	s_nop 0
	v_add_f32_e32 v111, 1.0, v111
	v_rcp_f32_e32 v111, v111
	s_nop 0
	v_mul_f32_e32 v110, v111, v110
	v_mul_f32_e32 v109, v110, v109
	v_cvt_pk_bf16_f32 v107, v108, v109
	v_lshlrev_b32_e32 v108, 16, v166
	v_mul_f32_e32 v109, 0x3d372713, v108
	v_mul_f32_e32 v109, v109, v108
	v_fma_f32 v109, v109, v108, v108
	v_mul_f32_e32 v109, 0x3f4c422a, v109
	v_mul_f32_e32 v109, -2.0, v109
	v_mul_f32_e32 v109, 0x3fb8aa3b, v109
	v_exp_f32_e32 v109, v109
	s_nop 0
	v_add_f32_e32 v109, 1.0, v109
	v_rcp_f32_e32 v109, v109
	s_nop 0
	v_mul_f32_e32 v108, v109, v108
	v_mul_f32_e32 v102, v108, v102
	v_and_b32_e32 v108, 0xffff0000, v166
	v_mul_f32_e32 v109, 0x3d372713, v108
	v_mul_f32_e32 v109, v109, v108
	v_fma_f32 v109, v109, v108, v108
	v_mul_f32_e32 v109, 0x3f4c422a, v109
	v_mul_f32_e32 v109, -2.0, v109
	v_mul_f32_e32 v109, 0x3fb8aa3b, v109
	v_exp_f32_e32 v109, v109
	s_nop 0
	v_add_f32_e32 v109, 1.0, v109
	v_rcp_f32_e32 v109, v109
	s_nop 0
	v_mul_f32_e32 v108, v109, v108
	v_mul_f32_e32 v103, v108, v103
	v_lshlrev_b32_e32 v108, 16, v167
	v_mul_f32_e32 v109, 0x3d372713, v108
	v_mul_f32_e32 v109, v109, v108
	v_fma_f32 v109, v109, v108, v108
	v_mul_f32_e32 v109, 0x3f4c422a, v109
	v_mul_f32_e32 v109, -2.0, v109
	v_mul_f32_e32 v109, 0x3fb8aa3b, v109
	v_exp_f32_e32 v109, v109
	s_nop 0
	v_add_f32_e32 v109, 1.0, v109
	v_rcp_f32_e32 v109, v109
	s_nop 0
	v_mul_f32_e32 v108, v109, v108
	v_mul_f32_e32 v104, v108, v104
	v_and_b32_e32 v108, 0xffff0000, v167
	v_mul_f32_e32 v109, 0x3d372713, v108
	v_mul_f32_e32 v109, v109, v108
	v_fma_f32 v109, v109, v108, v108
	v_mul_f32_e32 v109, 0x3f4c422a, v109
	v_mul_f32_e32 v109, -2.0, v109
	v_mul_f32_e32 v109, 0x3fb8aa3b, v109
	v_exp_f32_e32 v109, v109
	s_nop 0
	v_add_f32_e32 v109, 1.0, v109
	v_rcp_f32_e32 v109, v109
	s_nop 0
	v_mul_f32_e32 v108, v109, v108
	v_mul_f32_e32 v105, v108, v105
	v_cvt_pk_bf16_f32 v108, v102, v103
	v_lshlrev_b32_e32 v102, 16, v164
	v_mul_f32_e32 v103, 0x3d372713, v102
	v_mul_f32_e32 v103, v103, v102
	v_fma_f32 v103, v103, v102, v102
	v_mul_f32_e32 v103, 0x3f4c422a, v103
	v_mul_f32_e32 v103, -2.0, v103
	v_mul_f32_e32 v103, 0x3fb8aa3b, v103
	v_exp_f32_e32 v103, v103
	v_cvt_pk_bf16_f32 v109, v104, v105
	v_permlane16_swap_b32_e32 v106, v108
	v_add_f32_e32 v103, 1.0, v103
	v_rcp_f32_e32 v103, v103
	v_permlane16_swap_b32_e32 v107, v109
	global_store_dwordx4 v[52:53], v[106:109], off offset:320
	v_mul_f32_e32 v102, v103, v102
	v_mul_f32_e32 v98, v102, v98
	v_and_b32_e32 v102, 0xffff0000, v164
	v_mul_f32_e32 v103, 0x3d372713, v102
	v_mul_f32_e32 v103, v103, v102
	v_fma_f32 v103, v103, v102, v102
	v_mul_f32_e32 v103, 0x3f4c422a, v103
	v_mul_f32_e32 v103, -2.0, v103
	v_mul_f32_e32 v103, 0x3fb8aa3b, v103
	v_exp_f32_e32 v103, v103
	s_nop 0
	v_add_f32_e32 v103, 1.0, v103
	v_rcp_f32_e32 v103, v103
	s_nop 0
	v_mul_f32_e32 v102, v103, v102
	v_mul_f32_e32 v99, v102, v99
	v_lshlrev_b32_e32 v102, 16, v165
	v_mul_f32_e32 v103, 0x3d372713, v102
	v_mul_f32_e32 v103, v103, v102
	v_fma_f32 v103, v103, v102, v102
	v_mul_f32_e32 v103, 0x3f4c422a, v103
	v_mul_f32_e32 v103, -2.0, v103
	v_mul_f32_e32 v103, 0x3fb8aa3b, v103
	v_exp_f32_e32 v103, v103
	v_cvt_pk_bf16_f32 v98, v98, v99
	s_nop 0
	v_add_f32_e32 v103, 1.0, v103
	v_rcp_f32_e32 v103, v103
	s_nop 0
	v_mul_f32_e32 v102, v103, v102
	v_mul_f32_e32 v100, v102, v100
	v_and_b32_e32 v102, 0xffff0000, v165
	v_mul_f32_e32 v103, 0x3d372713, v102
	v_mul_f32_e32 v103, v103, v102
	v_fma_f32 v103, v103, v102, v102
	v_mul_f32_e32 v103, 0x3f4c422a, v103
	v_mul_f32_e32 v103, -2.0, v103
	v_mul_f32_e32 v103, 0x3fb8aa3b, v103
	v_exp_f32_e32 v103, v103
	s_nop 0
	v_add_f32_e32 v103, 1.0, v103
	v_rcp_f32_e32 v103, v103
	s_nop 0
	v_mul_f32_e32 v102, v103, v102
	v_mul_f32_e32 v101, v102, v101
	v_cvt_pk_bf16_f32 v99, v100, v101
	v_lshlrev_b32_e32 v100, 16, v192
	v_mul_f32_e32 v101, 0x3d372713, v100
	v_mul_f32_e32 v101, v101, v100
	v_fma_f32 v101, v101, v100, v100
	v_mul_f32_e32 v101, 0x3f4c422a, v101
	v_mul_f32_e32 v101, -2.0, v101
	v_mul_f32_e32 v101, 0x3fb8aa3b, v101
	v_exp_f32_e32 v101, v101
	s_nop 0
	v_add_f32_e32 v101, 1.0, v101
	v_rcp_f32_e32 v101, v101
	s_nop 0
	v_mul_f32_e32 v100, v101, v100
	v_mul_f32_e32 v94, v100, v94
	v_and_b32_e32 v100, 0xffff0000, v192
	v_mul_f32_e32 v101, 0x3d372713, v100
	v_mul_f32_e32 v101, v101, v100
	v_fma_f32 v101, v101, v100, v100
	v_mul_f32_e32 v101, 0x3f4c422a, v101
	v_mul_f32_e32 v101, -2.0, v101
	v_mul_f32_e32 v101, 0x3fb8aa3b, v101
	v_exp_f32_e32 v101, v101
	s_nop 0
	v_add_f32_e32 v101, 1.0, v101
	v_rcp_f32_e32 v101, v101
	s_nop 0
	v_mul_f32_e32 v100, v101, v100
	v_mul_f32_e32 v95, v100, v95
	v_lshlrev_b32_e32 v100, 16, v193
	v_mul_f32_e32 v101, 0x3d372713, v100
	v_mul_f32_e32 v101, v101, v100
	v_fma_f32 v101, v101, v100, v100
	v_mul_f32_e32 v101, 0x3f4c422a, v101
	v_mul_f32_e32 v101, -2.0, v101
	v_mul_f32_e32 v101, 0x3fb8aa3b, v101
	v_exp_f32_e32 v101, v101
	s_nop 0
	v_add_f32_e32 v101, 1.0, v101
	v_rcp_f32_e32 v101, v101
	s_nop 0
	v_mul_f32_e32 v100, v101, v100
	v_mul_f32_e32 v96, v100, v96
	v_and_b32_e32 v100, 0xffff0000, v193
	v_mul_f32_e32 v101, 0x3d372713, v100
	v_mul_f32_e32 v101, v101, v100
	v_fma_f32 v101, v101, v100, v100
	v_mul_f32_e32 v101, 0x3f4c422a, v101
	v_mul_f32_e32 v101, -2.0, v101
	v_mul_f32_e32 v101, 0x3fb8aa3b, v101
	v_exp_f32_e32 v101, v101
	s_nop 0
	v_add_f32_e32 v101, 1.0, v101
	v_rcp_f32_e32 v101, v101
	s_nop 0
	v_mul_f32_e32 v100, v101, v100
	v_mul_f32_e32 v97, v100, v97
	v_cvt_pk_bf16_f32 v100, v94, v95
	v_lshlrev_b32_e32 v94, 16, v190
	v_mul_f32_e32 v95, 0x3d372713, v94
	v_mul_f32_e32 v95, v95, v94
	v_fma_f32 v95, v95, v94, v94
	v_mul_f32_e32 v95, 0x3f4c422a, v95
	v_mul_f32_e32 v95, -2.0, v95
	v_mul_f32_e32 v95, 0x3fb8aa3b, v95
	v_exp_f32_e32 v95, v95
	v_cvt_pk_bf16_f32 v101, v96, v97
	v_permlane16_swap_b32_e32 v98, v100
	v_add_f32_e32 v95, 1.0, v95
	v_rcp_f32_e32 v95, v95
	v_permlane16_swap_b32_e32 v99, v101
	global_store_dwordx4 v[52:53], v[98:101], off offset:384
	v_mul_f32_e32 v94, v95, v94
	v_mul_f32_e32 v90, v94, v90
	v_and_b32_e32 v94, 0xffff0000, v190
	v_mul_f32_e32 v95, 0x3d372713, v94
	v_mul_f32_e32 v95, v95, v94
	v_fma_f32 v95, v95, v94, v94
	v_mul_f32_e32 v95, 0x3f4c422a, v95
	v_mul_f32_e32 v95, -2.0, v95
	v_mul_f32_e32 v95, 0x3fb8aa3b, v95
	v_exp_f32_e32 v95, v95
	s_nop 0
	v_add_f32_e32 v95, 1.0, v95
	v_rcp_f32_e32 v95, v95
	s_nop 0
	v_mul_f32_e32 v94, v95, v94
	v_mul_f32_e32 v91, v94, v91
	v_lshlrev_b32_e32 v94, 16, v191
	v_mul_f32_e32 v95, 0x3d372713, v94
	v_mul_f32_e32 v95, v95, v94
	v_fma_f32 v95, v95, v94, v94
	v_mul_f32_e32 v95, 0x3f4c422a, v95
	v_mul_f32_e32 v95, -2.0, v95
	v_mul_f32_e32 v95, 0x3fb8aa3b, v95
	v_exp_f32_e32 v95, v95
	v_cvt_pk_bf16_f32 v90, v90, v91
	s_nop 0
	v_add_f32_e32 v95, 1.0, v95
	v_rcp_f32_e32 v95, v95
	s_nop 0
	v_mul_f32_e32 v94, v95, v94
	v_mul_f32_e32 v92, v94, v92
	v_and_b32_e32 v94, 0xffff0000, v191
	v_mul_f32_e32 v95, 0x3d372713, v94
	v_mul_f32_e32 v95, v95, v94
	v_fma_f32 v95, v95, v94, v94
	v_mul_f32_e32 v95, 0x3f4c422a, v95
	v_mul_f32_e32 v95, -2.0, v95
	v_mul_f32_e32 v95, 0x3fb8aa3b, v95
	v_exp_f32_e32 v95, v95
	s_nop 0
	v_add_f32_e32 v95, 1.0, v95
	v_rcp_f32_e32 v95, v95
	s_nop 0
	v_mul_f32_e32 v94, v95, v94
	v_mul_f32_e32 v93, v94, v93
	v_cvt_pk_bf16_f32 v91, v92, v93
	v_lshlrev_b32_e32 v92, 16, v188
	v_mul_f32_e32 v93, 0x3d372713, v92
	v_mul_f32_e32 v93, v93, v92
	v_fma_f32 v93, v93, v92, v92
	v_mul_f32_e32 v93, 0x3f4c422a, v93
	v_mul_f32_e32 v93, -2.0, v93
	v_mul_f32_e32 v93, 0x3fb8aa3b, v93
	v_exp_f32_e32 v93, v93
	s_nop 0
	v_add_f32_e32 v93, 1.0, v93
	v_rcp_f32_e32 v93, v93
	s_nop 0
	v_mul_f32_e32 v92, v93, v92
	v_mul_f32_e32 v86, v92, v86
	v_and_b32_e32 v92, 0xffff0000, v188
	v_mul_f32_e32 v93, 0x3d372713, v92
	v_mul_f32_e32 v93, v93, v92
	v_fma_f32 v93, v93, v92, v92
	v_mul_f32_e32 v93, 0x3f4c422a, v93
	v_mul_f32_e32 v93, -2.0, v93
	v_mul_f32_e32 v93, 0x3fb8aa3b, v93
	v_exp_f32_e32 v93, v93
	s_nop 0
	v_add_f32_e32 v93, 1.0, v93
	v_rcp_f32_e32 v93, v93
	s_nop 0
	v_mul_f32_e32 v92, v93, v92
	v_mul_f32_e32 v87, v92, v87
	v_lshlrev_b32_e32 v92, 16, v189
	v_mul_f32_e32 v93, 0x3d372713, v92
	v_mul_f32_e32 v93, v93, v92
	v_fma_f32 v93, v93, v92, v92
	v_mul_f32_e32 v93, 0x3f4c422a, v93
	v_mul_f32_e32 v93, -2.0, v93
	v_mul_f32_e32 v93, 0x3fb8aa3b, v93
	v_exp_f32_e32 v93, v93
	s_nop 0
	v_add_f32_e32 v93, 1.0, v93
	v_rcp_f32_e32 v93, v93
	s_nop 0
	v_mul_f32_e32 v92, v93, v92
	v_mul_f32_e32 v88, v92, v88
	v_and_b32_e32 v92, 0xffff0000, v189
	v_mul_f32_e32 v93, 0x3d372713, v92
	v_mul_f32_e32 v93, v93, v92
	v_fma_f32 v93, v93, v92, v92
	v_mul_f32_e32 v93, 0x3f4c422a, v93
	v_mul_f32_e32 v93, -2.0, v93
	v_mul_f32_e32 v93, 0x3fb8aa3b, v93
	v_exp_f32_e32 v93, v93
	s_nop 0
	v_add_f32_e32 v93, 1.0, v93
	v_rcp_f32_e32 v93, v93
	s_nop 0
	v_mul_f32_e32 v92, v93, v92
	v_mul_f32_e32 v89, v92, v89
	v_cvt_pk_bf16_f32 v92, v86, v87
	v_cvt_pk_bf16_f32 v93, v88, v89
	s_nop 0
	v_permlane16_swap_b32_e32 v90, v92
	v_permlane16_swap_b32_e32 v91, v93
	global_store_dwordx4 v[52:53], v[90:93], off offset:448
